# P7 epilogue: second batch of residual loads hoisted next to first batch (into free v212-v243), vmcnt(8)/vmcnt(16)
# speedup vs baseline: 1.0038x; 1.0026x over previous
; __device__ __forceinline__ unsigned pk4_fp8(float a, float b, float c, float d) { int w = 0; w = __builtin_amdgcn_cvt_pk_fp8_f32(a, b, w, false); w = __builtin_amdgcn_cvt_pk_fp8_f32(c, d, w, true); return (unsigned)w; }
; __device__ __forceinline__ v4u pack8(const f32x4 a, const f32x4 b) { v4u w; w.x = cvt_pk_bf16(a[0], a[1]); w.y = cvt_pk_bf16(a[2], a[3]); w.z = cvt_pk_bf16(b[0], b[1]); w.w = cvt_pk_bf16(b[2], b[3]); return w; }
;     __device__ __forceinline__ void operator()(const Acc& acc, const Unit& u, int wr, int wc, int fr, int fq) const {
;         const int col0 = u.pn * 256 + wc * 32 + 8 * fq;
; #pragma unroll
;         for (int ai = 0; ai < 2; ++ai) { v4u xv[4][2];
; #pragma unroll
;             for (int m = 0; m < 4; ++m) { const size_t off = (size_t)EPI_ROWS(ai, m) * DM + col0;
; #pragma unroll
;                 for (int bj = 0; bj < 2; ++bj) xv[m][bj] = *(const v4u*)(x1b + off + bj * 128); }
; #pragma unroll
;             for (int m = 0; m < 4; ++m) { const size_t off = (size_t)EPI_ROWS(ai, m) * DM + col0;
; #pragma unroll
;                 for (int bj = 0; bj < 2; ++bj) { const v4u w = xv[m][bj];
;                     const f32x4 v0 = (f32x4){__uint_as_float(w.x << 16), __uint_as_float(w.x & 0xffff0000u), __uint_as_float(w.y << 16), __uint_as_float(w.y & 0xffff0000u)} + acc[ai][bj][m][0],
;                                 v1 = (f32x4){__uint_as_float(w.z << 16), __uint_as_float(w.z & 0xffff0000u), __uint_as_float(w.w << 16), __uint_as_float(w.w & 0xffff0000u)} + acc[ai][bj][m][1];
;                     *(v4u*)(x2 + off + bj * 128) = pack8(v0, v1); v2u o; o.x = pk4_fp8(v0[0], v0[1], v0[2], v0[3]); o.y = pk4_fp8(v1[0], v1[1], v1[2], v1[3]); *(v2u*)(x2b + off + bj * 128) = o; } } }
.LBB5_1408:
	s_lshl_b32 s35, s59, 8
	v_mov_b32_e32 v130, v151
	v_mov_b32_e32 v131, v152
	s_or_b32 s35, s35, s53
	v_mov_b32_e32 v182, v139
	v_lshl_add_u32 v140, v131, 3, s35
	s_lshl_b32 s35, s40, 8
	s_add_i32 s35, s35, s52
	v_add_u32_e32 v144, s35, v130
	v_ashrrev_i32_e32 v141, 31, v140
	v_ashrrev_i32_e32 v145, 31, v144
	v_lshl_add_u64 v[142:143], v[140:141], 1, s[6:7]
	v_lshlrev_b64 v[130:131], 12, v[144:145]
	v_lshl_add_u64 v[130:131], v[142:143], 0, v[130:131]
	global_load_dwordx4 v[158:161], v[130:131], off
	global_load_dwordx4 v[162:165], v[130:131], off offset:256
	v_add_u32_e32 v130, 16, v144
	v_ashrrev_i32_e32 v131, 31, v130
	v_lshlrev_b64 v[132:133], 12, v[130:131]
	v_lshl_add_u64 v[132:133], v[142:143], 0, v[132:133]
	global_load_dwordx4 v[166:169], v[132:133], off
	global_load_dwordx4 v[170:173], v[132:133], off offset:256
	v_add_u32_e32 v186, 32, v144
	v_add_u32_e32 v146, 48, v144
	v_ashrrev_i32_e32 v187, 31, v186
	v_ashrrev_i32_e32 v147, 31, v146
	v_lshlrev_b64 v[134:135], 11, v[144:145]
	v_lshlrev_b64 v[136:137], 12, v[186:187]
	v_lshlrev_b64 v[174:175], 12, v[146:147]
	v_lshl_add_u64 v[134:135], v[134:135], 0, v[140:141]
	v_lshlrev_b64 v[130:131], 11, v[130:131]
	v_lshl_add_u64 v[132:133], v[142:143], 0, v[136:137]
	v_lshl_add_u64 v[188:189], v[142:143], 0, v[174:175]
	v_lshl_add_u64 v[190:191], v[134:135], 1, s[8:9]
	v_lshl_add_u64 v[192:193], s[10:11], 0, v[134:135]
	v_lshl_add_u64 v[194:195], v[130:131], 0, v[140:141]
	global_load_dwordx4 v[174:177], v[132:133], off
	global_load_dwordx4 v[178:181], v[132:133], off offset:256
	global_load_dwordx4 v[134:137], v[188:189], off
	s_nop 0
	global_load_dwordx4 v[130:133], v[188:189], off offset:256
	v_add_u32_e32 v210, 0x80, v144
	v_ashrrev_i32_e32 v211, 31, v210
	v_lshlrev_b64 v[244:245], 12, v[210:211]
	v_lshl_add_u64 v[244:245], v[142:143], 0, v[244:245]
	global_load_dwordx4 v[212:215], v[244:245], off
	global_load_dwordx4 v[216:219], v[244:245], off offset:256
	v_add_u32_e32 v210, 0x90, v144
	v_ashrrev_i32_e32 v211, 31, v210
	v_lshlrev_b64 v[246:247], 12, v[210:211]
	v_lshl_add_u64 v[246:247], v[142:143], 0, v[246:247]
	global_load_dwordx4 v[220:223], v[246:247], off
	global_load_dwordx4 v[224:227], v[246:247], off offset:256
	v_add_u32_e32 v210, 0xa0, v144
	v_ashrrev_i32_e32 v211, 31, v210
	v_lshlrev_b64 v[248:249], 12, v[210:211]
	v_lshl_add_u64 v[248:249], v[142:143], 0, v[248:249]
	global_load_dwordx4 v[228:231], v[248:249], off
	global_load_dwordx4 v[232:235], v[248:249], off offset:256
	v_add_u32_e32 v210, 0xb0, v144
	v_ashrrev_i32_e32 v211, 31, v210
	v_lshlrev_b64 v[250:251], 12, v[210:211]
	v_lshl_add_u64 v[250:251], v[142:143], 0, v[250:251]
	global_load_dwordx4 v[236:239], v[250:251], off
	global_load_dwordx4 v[240:243], v[250:251], off offset:256
	v_mov_b32_e32 v183, v139
	v_mov_b32_e32 v184, v139
	v_mov_b32_e32 v185, v139
	v_readlane_b32 s60, v253, 42
	v_readlane_b32 s64, v253, 46
	v_readlane_b32 s65, v253, 47
	v_readlane_b32 s72, v253, 54
	v_readlane_b32 s73, v253, 55
	s_andn2_b64 vcc, exec, s[18:19]
	s_mov_b64 s[18:19], -1
	s_mov_b64 s[64:65], s[72:73]
	v_readlane_b32 s61, v253, 43
	v_readlane_b32 s62, v253, 44
	v_readlane_b32 s63, v253, 45
	v_readlane_b32 s66, v253, 48
	v_readlane_b32 s67, v253, 49
	v_readlane_b32 s68, v253, 50
	v_readlane_b32 s69, v253, 51
	v_readlane_b32 s70, v253, 52
	v_readlane_b32 s71, v253, 53
	v_readlane_b32 s74, v253, 56
	v_readlane_b32 s75, v253, 57
	s_waitcnt vmcnt(8)
	v_lshlrev_b32_e32 v188, 16, v158
	v_and_b32_e32 v189, 0xffff0000, v158
	v_lshlrev_b32_e32 v196, 16, v160
	v_and_b32_e32 v197, 0xffff0000, v160
	v_pk_add_f32 v[126:127], v[126:127], v[188:189]
	v_pk_add_f32 v[122:123], v[122:123], v[196:197]
	v_lshlrev_b32_e32 v160, 16, v161
	v_and_b32_e32 v161, 0xffff0000, v161
	v_lshlrev_b32_e32 v200, 16, v162
	v_and_b32_e32 v201, 0xffff0000, v162
	v_lshlrev_b32_e32 v202, 16, v164
	v_and_b32_e32 v203, 0xffff0000, v164
	v_cvt_pk_fp8_f32 v182, v126, v127
	v_cvt_pk_fp8_f32 v183, v122, v123
	v_pk_add_f32 v[124:125], v[124:125], v[160:161]
	v_pk_add_f32 v[118:119], v[118:119], v[200:201]
	v_pk_add_f32 v[160:161], v[110:111], v[202:203]
	v_lshlrev_b32_e32 v158, 16, v159
	v_and_b32_e32 v159, 0xffff0000, v159
	v_cvt_pk_fp8_f32 v184, v118, v119
	v_cvt_pk_fp8_f32 v185, v160, v161
	v_pk_add_f32 v[128:129], v[128:129], v[158:159]
	v_lshlrev_b32_e32 v162, 16, v163
	v_and_b32_e32 v163, 0xffff0000, v163
	v_lshlrev_b32_e32 v164, 16, v165
	v_and_b32_e32 v165, 0xffff0000, v165
	v_cvt_pk_fp8_f32 v182, v128, v129 op_sel:[0,0,1]
	v_cvt_pk_fp8_f32 v183, v124, v125 op_sel:[0,0,1]
	v_pk_add_f32 v[120:121], v[120:121], v[162:163]
	v_pk_add_f32 v[158:159], v[112:113], v[164:165]
	v_cvt_pk_fp8_f32 v184, v120, v121 op_sel:[0,0,1]
	v_cvt_pk_fp8_f32 v185, v158, v159 op_sel:[0,0,1]
	v_cvt_pk_bf16_f32 v110, v126, v127
	v_cvt_pk_bf16_f32 v111, v128, v129
	v_cvt_pk_bf16_f32 v112, v122, v123
	v_cvt_pk_bf16_f32 v113, v124, v125
	v_lshlrev_b32_e32 v162, 16, v166
	v_and_b32_e32 v163, 0xffff0000, v166
	v_lshlrev_b32_e32 v164, 16, v167
	v_and_b32_e32 v165, 0xffff0000, v167
	v_lshlrev_b32_e32 v166, 16, v168
	v_and_b32_e32 v167, 0xffff0000, v168
	v_lshlrev_b32_e32 v168, 16, v169
	v_and_b32_e32 v169, 0xffff0000, v169
	global_store_dwordx4 v[190:191], v[110:113], off
	global_store_dwordx2 v[192:193], v[182:183], off
	v_pk_add_f32 v[114:115], v[114:115], v[162:163]
	v_cvt_pk_bf16_f32 v110, v118, v119
	v_cvt_pk_bf16_f32 v111, v120, v121
	v_cvt_pk_bf16_f32 v112, v160, v161
	v_cvt_pk_bf16_f32 v113, v158, v159
	global_store_dwordx4 v[190:191], v[110:113], off offset:256
	global_store_dwordx2 v[192:193], v[184:185], off offset:128
	v_pk_add_f32 v[116:117], v[116:117], v[164:165]
; __device__ __forceinline__ unsigned pk4_fp8(float a, float b, float c, float d) { int w = 0; w = __builtin_amdgcn_cvt_pk_fp8_f32(a, b, w, false); w = __builtin_amdgcn_cvt_pk_fp8_f32(c, d, w, true); return (unsigned)w; }
; __device__ __forceinline__ v4u pack8(const f32x4 a, const f32x4 b) { v4u w; w.x = cvt_pk_bf16(a[0], a[1]); w.y = cvt_pk_bf16(a[2], a[3]); w.z = cvt_pk_bf16(b[0], b[1]); w.w = cvt_pk_bf16(b[2], b[3]); return w; }
;     __device__ __forceinline__ void operator()(const Acc& acc, const Unit& u, int wr, int wc, int fr, int fq) const {
;     ...
;             for (int m = 0; m < 4; ++m) { const size_t off = (size_t)EPI_ROWS(ai, m) * DM + col0;
; #pragma unroll
;                 for (int bj = 0; bj < 2; ++bj) { const v4u w = xv[m][bj];
;                     const f32x4 v0 = (f32x4){__uint_as_float(w.x << 16), __uint_as_float(w.x & 0xffff0000u), __uint_as_float(w.y << 16), __uint_as_float(w.y & 0xffff0000u)} + acc[ai][bj][m][0],
;                                 v1 = (f32x4){__uint_as_float(w.z << 16), __uint_as_float(w.z & 0xffff0000u), __uint_as_float(w.w << 16), __uint_as_float(w.w & 0xffff0000u)} + acc[ai][bj][m][1];
;                     *(v4u*)(x2 + off + bj * 128) = pack8(v0, v1); v2u o; o.x = pk4_fp8(v0[0], v0[1], v0[2], v0[3]); o.y = pk4_fp8(v1[0], v1[1], v1[2], v1[3]); *(v2u*)(x2b + off + bj * 128) = o; } } }
	v_pk_add_f32 v[110:111], v[108:109], v[168:169]
	v_pk_add_f32 v[108:109], v[106:107], v[166:167]
	v_mov_b32_e32 v112, v139
	v_mov_b32_e32 v113, v139
	v_cvt_pk_fp8_f32 v112, v114, v115
	v_cvt_pk_fp8_f32 v113, v108, v109
	v_cvt_pk_bf16_f32 v106, v114, v115
	v_cvt_pk_bf16_f32 v107, v116, v117
	v_cvt_pk_fp8_f32 v112, v116, v117 op_sel:[0,0,1]
	v_cvt_pk_fp8_f32 v113, v110, v111 op_sel:[0,0,1]
	v_cvt_pk_bf16_f32 v108, v108, v109
	v_cvt_pk_bf16_f32 v109, v110, v111
	v_lshl_add_u64 v[110:111], v[194:195], 1, s[8:9]
	global_store_dwordx4 v[110:111], v[106:109], off
	s_nop 1
	v_lshl_add_u64 v[106:107], s[10:11], 0, v[194:195]
	global_store_dwordx2 v[106:107], v[112:113], off
	v_lshlrev_b32_e32 v108, 16, v170
	v_and_b32_e32 v109, 0xffff0000, v170
	v_lshlrev_b32_e32 v112, 16, v171
	v_and_b32_e32 v113, 0xffff0000, v171
	v_pk_add_f32 v[104:105], v[104:105], v[112:113]
	v_pk_add_f32 v[102:103], v[102:103], v[108:109]
	v_lshlrev_b32_e32 v108, 16, v172
	v_and_b32_e32 v109, 0xffff0000, v172
	v_lshlrev_b32_e32 v112, 16, v173
	v_and_b32_e32 v113, 0xffff0000, v173
	v_pk_add_f32 v[112:113], v[100:101], v[112:113]
	v_pk_add_f32 v[100:101], v[98:99], v[108:109]
	v_mov_b32_e32 v108, v139
	v_mov_b32_e32 v109, v139
	v_cvt_pk_fp8_f32 v108, v102, v103
	v_cvt_pk_fp8_f32 v109, v100, v101
	v_cvt_pk_bf16_f32 v98, v102, v103
	v_cvt_pk_bf16_f32 v99, v104, v105
	v_cvt_pk_fp8_f32 v108, v104, v105 op_sel:[0,0,1]
	v_cvt_pk_fp8_f32 v109, v112, v113 op_sel:[0,0,1]
	v_cvt_pk_bf16_f32 v100, v100, v101
	v_cvt_pk_bf16_f32 v101, v112, v113
	global_store_dwordx4 v[110:111], v[98:101], off offset:256
	global_store_dwordx2 v[106:107], v[108:109], off offset:128
	v_lshlrev_b32_e32 v102, 16, v175
	v_lshlrev_b32_e32 v100, 16, v174
	v_and_b32_e32 v101, 0xffff0000, v174
	v_and_b32_e32 v103, 0xffff0000, v175
	v_pk_add_f32 v[96:97], v[96:97], v[102:103]
	v_pk_add_f32 v[94:95], v[94:95], v[100:101]
	v_lshlrev_b32_e32 v100, 16, v176
	v_and_b32_e32 v101, 0xffff0000, v176
	v_lshlrev_b32_e32 v102, 16, v177
	v_and_b32_e32 v103, 0xffff0000, v177
	v_pk_add_f32 v[102:103], v[92:93], v[102:103]
	v_pk_add_f32 v[92:93], v[90:91], v[100:101]
	v_mov_b32_e32 v100, v139
	v_cvt_pk_fp8_f32 v100, v94, v95
	v_lshlrev_b64 v[98:99], 11, v[186:187]
	v_lshl_add_u64 v[98:99], v[98:99], 0, v[140:141]
	v_mov_b32_e32 v101, v139
	v_cvt_pk_bf16_f32 v90, v94, v95
	v_cvt_pk_bf16_f32 v91, v96, v97
	v_cvt_pk_fp8_f32 v101, v92, v93
	v_cvt_pk_bf16_f32 v92, v92, v93
	v_cvt_pk_bf16_f32 v93, v102, v103
	v_lshl_add_u64 v[94:95], v[98:99], 1, s[8:9]
	v_cvt_pk_fp8_f32 v100, v96, v97 op_sel:[0,0,1]
	global_store_dwordx4 v[94:95], v[90:93], off
	v_lshlrev_b32_e32 v96, 16, v179
	v_and_b32_e32 v97, 0xffff0000, v179
	v_lshlrev_b32_e32 v92, 16, v178
	v_and_b32_e32 v93, 0xffff0000, v178
	v_pk_add_f32 v[88:89], v[88:89], v[96:97]
	v_pk_add_f32 v[86:87], v[86:87], v[92:93]
	v_lshlrev_b32_e32 v92, 16, v180
	v_and_b32_e32 v93, 0xffff0000, v180
	v_lshlrev_b32_e32 v96, 16, v181
	v_and_b32_e32 v97, 0xffff0000, v181
	v_pk_add_f32 v[96:97], v[84:85], v[96:97]
	v_pk_add_f32 v[84:85], v[82:83], v[92:93]
	v_mov_b32_e32 v92, v139
	v_mov_b32_e32 v93, v139
	v_cvt_pk_fp8_f32 v92, v86, v87
	v_cvt_pk_fp8_f32 v93, v84, v85
	v_cvt_pk_fp8_f32 v101, v102, v103 op_sel:[0,0,1]
	v_lshl_add_u64 v[90:91], s[10:11], 0, v[98:99]
	v_cvt_pk_fp8_f32 v92, v88, v89 op_sel:[0,0,1]
	v_cvt_pk_fp8_f32 v93, v96, v97 op_sel:[0,0,1]
	global_store_dwordx2 v[90:91], v[100:101], off
	v_cvt_pk_bf16_f32 v82, v86, v87
	v_cvt_pk_bf16_f32 v83, v88, v89
	v_cvt_pk_bf16_f32 v84, v84, v85
	v_cvt_pk_bf16_f32 v85, v96, v97
	global_store_dwordx4 v[94:95], v[82:85], off offset:256
	global_store_dwordx2 v[90:91], v[92:93], off offset:128
	v_lshlrev_b32_e32 v86, 16, v135
	v_lshlrev_b32_e32 v84, 16, v134
	v_and_b32_e32 v85, 0xffff0000, v134
	v_and_b32_e32 v87, 0xffff0000, v135
	v_pk_add_f32 v[80:81], v[80:81], v[86:87]
	v_pk_add_f32 v[78:79], v[78:79], v[84:85]
	v_lshlrev_b32_e32 v84, 16, v136
	v_and_b32_e32 v85, 0xffff0000, v136
	v_lshlrev_b32_e32 v86, 16, v137
	v_and_b32_e32 v87, 0xffff0000, v137
	v_pk_add_f32 v[86:87], v[76:77], v[86:87]
	v_pk_add_f32 v[76:77], v[74:75], v[84:85]
	v_mov_b32_e32 v84, v139
	v_cvt_pk_fp8_f32 v84, v78, v79
	v_lshlrev_b64 v[82:83], 11, v[146:147]
	v_lshl_add_u64 v[82:83], v[82:83], 0, v[140:141]
	v_mov_b32_e32 v85, v139
	v_cvt_pk_bf16_f32 v74, v78, v79
	v_cvt_pk_bf16_f32 v75, v80, v81
	v_cvt_pk_fp8_f32 v85, v76, v77
	v_cvt_pk_bf16_f32 v76, v76, v77
	v_cvt_pk_bf16_f32 v77, v86, v87
	v_lshl_add_u64 v[78:79], v[82:83], 1, s[8:9]
	v_cvt_pk_fp8_f32 v84, v80, v81 op_sel:[0,0,1]
	global_store_dwordx4 v[78:79], v[74:77], off
	v_lshlrev_b32_e32 v80, 16, v131
	v_and_b32_e32 v81, 0xffff0000, v131
	v_lshlrev_b32_e32 v76, 16, v130
	v_and_b32_e32 v77, 0xffff0000, v130
	v_pk_add_f32 v[72:73], v[72:73], v[80:81]
	v_pk_add_f32 v[70:71], v[70:71], v[76:77]
	v_lshlrev_b32_e32 v76, 16, v132
	v_and_b32_e32 v77, 0xffff0000, v132
	v_lshlrev_b32_e32 v80, 16, v133
	v_and_b32_e32 v81, 0xffff0000, v133
	v_pk_add_f32 v[80:81], v[68:69], v[80:81]
	v_pk_add_f32 v[68:69], v[66:67], v[76:77]
	v_mov_b32_e32 v76, v139
	v_mov_b32_e32 v77, v139
	v_cvt_pk_fp8_f32 v76, v70, v71
	v_cvt_pk_fp8_f32 v77, v68, v69
	v_cvt_pk_fp8_f32 v85, v86, v87 op_sel:[0,0,1]
	v_lshl_add_u64 v[74:75], s[10:11], 0, v[82:83]
	v_cvt_pk_fp8_f32 v76, v72, v73 op_sel:[0,0,1]
	v_cvt_pk_fp8_f32 v77, v80, v81 op_sel:[0,0,1]
	v_add_u32_e32 v100, 0x80, v144
	global_store_dwordx2 v[74:75], v[84:85], off
	v_cvt_pk_bf16_f32 v66, v70, v71
	v_cvt_pk_bf16_f32 v67, v72, v73
	v_cvt_pk_bf16_f32 v68, v68, v69
	v_cvt_pk_bf16_f32 v69, v80, v81
	v_ashrrev_i32_e32 v101, 31, v100
	global_store_dwordx4 v[78:79], v[66:69], off offset:256
	global_store_dwordx2 v[74:75], v[76:77], off offset:128
	v_add_u32_e32 v102, 0x90, v144
	v_ashrrev_i32_e32 v103, 31, v102
	v_add_u32_e32 v104, 0xa0, v144
	v_ashrrev_i32_e32 v105, 31, v104
	v_add_u32_e32 v82, 0xb0, v144
	v_ashrrev_i32_e32 v83, 31, v82
	v_lshlrev_b64 v[100:101], 11, v[100:101]
	v_lshl_add_u64 v[100:101], v[100:101], 0, v[140:141]
	s_waitcnt vmcnt(16)
; __device__ __forceinline__ unsigned pk4_fp8(float a, float b, float c, float d) { int w = 0; w = __builtin_amdgcn_cvt_pk_fp8_f32(a, b, w, false); w = __builtin_amdgcn_cvt_pk_fp8_f32(c, d, w, true); return (unsigned)w; }
; __device__ __forceinline__ v4u pack8(const f32x4 a, const f32x4 b) { v4u w; w.x = cvt_pk_bf16(a[0], a[1]); w.y = cvt_pk_bf16(a[2], a[3]); w.z = cvt_pk_bf16(b[0], b[1]); w.w = cvt_pk_bf16(b[2], b[3]); return w; }
;     __device__ __forceinline__ void operator()(const Acc& acc, const Unit& u, int wr, int wc, int fr, int fq) const {
;     ...
;             for (int m = 0; m < 4; ++m) { const size_t off = (size_t)EPI_ROWS(ai, m) * DM + col0;
; #pragma unroll
;                 for (int bj = 0; bj < 2; ++bj) { const v4u w = xv[m][bj];
;                     const f32x4 v0 = (f32x4){__uint_as_float(w.x << 16), __uint_as_float(w.x & 0xffff0000u), __uint_as_float(w.y << 16), __uint_as_float(w.y & 0xffff0000u)} + acc[ai][bj][m][0],
;                                 v1 = (f32x4){__uint_as_float(w.z << 16), __uint_as_float(w.z & 0xffff0000u), __uint_as_float(w.w << 16), __uint_as_float(w.w & 0xffff0000u)} + acc[ai][bj][m][1];
;                     *(v4u*)(x2 + off + bj * 128) = pack8(v0, v1); v2u o; o.x = pk4_fp8(v0[0], v0[1], v0[2], v0[3]); o.y = pk4_fp8(v1[0], v1[1], v1[2], v1[3]); *(v2u*)(x2b + off + bj * 128) = o; } } }
	v_lshlrev_b32_e32 v106, 16, v212
	v_and_b32_e32 v107, 0xffff0000, v212
	v_lshlrev_b32_e32 v84, 16, v213
	v_and_b32_e32 v85, 0xffff0000, v213
	v_pk_add_f32 v[64:65], v[64:65], v[84:85]
	v_lshlrev_b32_e32 v84, 16, v214
	v_and_b32_e32 v85, 0xffff0000, v214
	v_lshlrev_b32_e32 v86, 16, v215
	v_and_b32_e32 v87, 0xffff0000, v215
	v_pk_add_f32 v[62:63], v[62:63], v[106:107]
	v_pk_add_f32 v[86:87], v[60:61], v[86:87]
	v_pk_add_f32 v[60:61], v[58:59], v[84:85]
	v_mov_b32_e32 v84, v139
	v_cvt_pk_fp8_f32 v84, v62, v63
	v_mov_b32_e32 v85, v139
	v_cvt_pk_bf16_f32 v58, v62, v63
	v_cvt_pk_bf16_f32 v59, v64, v65
	v_cvt_pk_fp8_f32 v85, v60, v61
	v_cvt_pk_bf16_f32 v60, v60, v61
	v_cvt_pk_bf16_f32 v61, v86, v87
	v_lshl_add_u64 v[62:63], v[100:101], 1, s[8:9]
	v_cvt_pk_fp8_f32 v84, v64, v65 op_sel:[0,0,1]
	global_store_dwordx4 v[62:63], v[58:61], off
	v_lshlrev_b32_e32 v64, 16, v217
	v_and_b32_e32 v65, 0xffff0000, v217
	v_lshlrev_b32_e32 v60, 16, v216
	v_and_b32_e32 v61, 0xffff0000, v216
	v_pk_add_f32 v[56:57], v[56:57], v[64:65]
	v_pk_add_f32 v[54:55], v[54:55], v[60:61]
	v_lshlrev_b32_e32 v60, 16, v218
	v_and_b32_e32 v61, 0xffff0000, v218
	v_lshlrev_b32_e32 v64, 16, v219
	v_and_b32_e32 v65, 0xffff0000, v219
	v_pk_add_f32 v[64:65], v[52:53], v[64:65]
	v_pk_add_f32 v[52:53], v[50:51], v[60:61]
	v_mov_b32_e32 v60, v139
	v_mov_b32_e32 v61, v139
	v_cvt_pk_fp8_f32 v60, v54, v55
	v_cvt_pk_fp8_f32 v61, v52, v53
	v_cvt_pk_fp8_f32 v85, v86, v87 op_sel:[0,0,1]
	v_lshl_add_u64 v[58:59], s[10:11], 0, v[100:101]
	v_cvt_pk_fp8_f32 v60, v56, v57 op_sel:[0,0,1]
	v_cvt_pk_fp8_f32 v61, v64, v65 op_sel:[0,0,1]
	global_store_dwordx2 v[58:59], v[84:85], off
	v_cvt_pk_bf16_f32 v50, v54, v55
	v_cvt_pk_bf16_f32 v51, v56, v57
	v_cvt_pk_bf16_f32 v52, v52, v53
	v_cvt_pk_bf16_f32 v53, v64, v65
	global_store_dwordx4 v[62:63], v[50:53], off offset:256
	global_store_dwordx2 v[58:59], v[60:61], off offset:128
	v_lshlrev_b32_e32 v54, 16, v221
	v_lshlrev_b32_e32 v52, 16, v220
	v_and_b32_e32 v53, 0xffff0000, v220
	v_and_b32_e32 v55, 0xffff0000, v221
	v_pk_add_f32 v[48:49], v[48:49], v[54:55]
	v_pk_add_f32 v[46:47], v[46:47], v[52:53]
	v_lshlrev_b32_e32 v52, 16, v222
	v_and_b32_e32 v53, 0xffff0000, v222
	v_lshlrev_b32_e32 v54, 16, v223
	v_and_b32_e32 v55, 0xffff0000, v223
	v_pk_add_f32 v[54:55], v[44:45], v[54:55]
	v_pk_add_f32 v[44:45], v[42:43], v[52:53]
	v_mov_b32_e32 v52, v139
	v_cvt_pk_fp8_f32 v52, v46, v47
	v_lshlrev_b64 v[50:51], 11, v[102:103]
	v_lshl_add_u64 v[50:51], v[50:51], 0, v[140:141]
	v_mov_b32_e32 v53, v139
	v_cvt_pk_bf16_f32 v42, v46, v47
	v_cvt_pk_bf16_f32 v43, v48, v49
	v_cvt_pk_fp8_f32 v53, v44, v45
	v_cvt_pk_bf16_f32 v44, v44, v45
	v_cvt_pk_bf16_f32 v45, v54, v55
	v_lshl_add_u64 v[46:47], v[50:51], 1, s[8:9]
	v_cvt_pk_fp8_f32 v52, v48, v49 op_sel:[0,0,1]
	global_store_dwordx4 v[46:47], v[42:45], off
	v_lshlrev_b32_e32 v48, 16, v225
	v_and_b32_e32 v49, 0xffff0000, v225
	v_lshlrev_b32_e32 v44, 16, v224
	v_and_b32_e32 v45, 0xffff0000, v224
	v_pk_add_f32 v[40:41], v[40:41], v[48:49]
	v_pk_add_f32 v[38:39], v[38:39], v[44:45]
	v_lshlrev_b32_e32 v44, 16, v226
	v_and_b32_e32 v45, 0xffff0000, v226
	v_lshlrev_b32_e32 v48, 16, v227
	v_and_b32_e32 v49, 0xffff0000, v227
	v_pk_add_f32 v[48:49], v[36:37], v[48:49]
	v_pk_add_f32 v[36:37], v[34:35], v[44:45]
	v_mov_b32_e32 v44, v139
	v_mov_b32_e32 v45, v139
	v_cvt_pk_fp8_f32 v44, v38, v39
	v_cvt_pk_fp8_f32 v45, v36, v37
	v_cvt_pk_fp8_f32 v53, v54, v55 op_sel:[0,0,1]
	v_lshl_add_u64 v[42:43], s[10:11], 0, v[50:51]
	v_cvt_pk_fp8_f32 v44, v40, v41 op_sel:[0,0,1]
	v_cvt_pk_fp8_f32 v45, v48, v49 op_sel:[0,0,1]
	global_store_dwordx2 v[42:43], v[52:53], off
	v_cvt_pk_bf16_f32 v34, v38, v39
	v_cvt_pk_bf16_f32 v35, v40, v41
	v_cvt_pk_bf16_f32 v36, v36, v37
	v_cvt_pk_bf16_f32 v37, v48, v49
	global_store_dwordx4 v[46:47], v[34:37], off offset:256
	global_store_dwordx2 v[42:43], v[44:45], off offset:128
	v_lshlrev_b32_e32 v38, 16, v229
	v_lshlrev_b32_e32 v36, 16, v228
; __device__ __forceinline__ unsigned pk4_fp8(float a, float b, float c, float d) { int w = 0; w = __builtin_amdgcn_cvt_pk_fp8_f32(a, b, w, false); w = __builtin_amdgcn_cvt_pk_fp8_f32(c, d, w, true); return (unsigned)w; }
; __device__ __forceinline__ v4u pack8(const f32x4 a, const f32x4 b) { v4u w; w.x = cvt_pk_bf16(a[0], a[1]); w.y = cvt_pk_bf16(a[2], a[3]); w.z = cvt_pk_bf16(b[0], b[1]); w.w = cvt_pk_bf16(b[2], b[3]); return w; }
;     __device__ __forceinline__ void operator()(const Acc& acc, const Unit& u, int wr, int wc, int fr, int fq) const {
;     ...
;             for (int m = 0; m < 4; ++m) { const size_t off = (size_t)EPI_ROWS(ai, m) * DM + col0;
; #pragma unroll
;                 for (int bj = 0; bj < 2; ++bj) { const v4u w = xv[m][bj];
;                     const f32x4 v0 = (f32x4){__uint_as_float(w.x << 16), __uint_as_float(w.x & 0xffff0000u), __uint_as_float(w.y << 16), __uint_as_float(w.y & 0xffff0000u)} + acc[ai][bj][m][0],
;                                 v1 = (f32x4){__uint_as_float(w.z << 16), __uint_as_float(w.z & 0xffff0000u), __uint_as_float(w.w << 16), __uint_as_float(w.w & 0xffff0000u)} + acc[ai][bj][m][1];
;                     *(v4u*)(x2 + off + bj * 128) = pack8(v0, v1); v2u o; o.x = pk4_fp8(v0[0], v0[1], v0[2], v0[3]); o.y = pk4_fp8(v1[0], v1[1], v1[2], v1[3]); *(v2u*)(x2b + off + bj * 128) = o; } } }
	v_and_b32_e32 v37, 0xffff0000, v228
	v_and_b32_e32 v39, 0xffff0000, v229
	v_pk_add_f32 v[32:33], v[32:33], v[38:39]
	v_pk_add_f32 v[30:31], v[30:31], v[36:37]
	v_lshlrev_b32_e32 v36, 16, v230
	v_and_b32_e32 v37, 0xffff0000, v230
	v_lshlrev_b32_e32 v38, 16, v231
	v_and_b32_e32 v39, 0xffff0000, v231
	v_pk_add_f32 v[38:39], v[28:29], v[38:39]
	v_pk_add_f32 v[28:29], v[26:27], v[36:37]
	v_mov_b32_e32 v36, v139
	v_cvt_pk_fp8_f32 v36, v30, v31
	v_lshlrev_b64 v[34:35], 11, v[104:105]
	v_lshl_add_u64 v[34:35], v[34:35], 0, v[140:141]
	v_mov_b32_e32 v37, v139
	v_cvt_pk_bf16_f32 v26, v30, v31
	v_cvt_pk_bf16_f32 v27, v32, v33
	v_cvt_pk_fp8_f32 v37, v28, v29
	v_cvt_pk_bf16_f32 v28, v28, v29
	v_cvt_pk_bf16_f32 v29, v38, v39
	v_lshl_add_u64 v[30:31], v[34:35], 1, s[8:9]
	v_cvt_pk_fp8_f32 v36, v32, v33 op_sel:[0,0,1]
	global_store_dwordx4 v[30:31], v[26:29], off
	v_lshlrev_b32_e32 v32, 16, v233
	v_and_b32_e32 v33, 0xffff0000, v233
	v_lshlrev_b32_e32 v28, 16, v232
	v_and_b32_e32 v29, 0xffff0000, v232
	v_pk_add_f32 v[24:25], v[24:25], v[32:33]
	v_pk_add_f32 v[22:23], v[22:23], v[28:29]
	v_lshlrev_b32_e32 v28, 16, v234
	v_and_b32_e32 v29, 0xffff0000, v234
	v_lshlrev_b32_e32 v32, 16, v235
	v_and_b32_e32 v33, 0xffff0000, v235
	v_pk_add_f32 v[32:33], v[20:21], v[32:33]
	v_pk_add_f32 v[20:21], v[18:19], v[28:29]
	v_mov_b32_e32 v28, v139
	v_mov_b32_e32 v29, v139
	v_cvt_pk_fp8_f32 v28, v22, v23
	v_cvt_pk_fp8_f32 v29, v20, v21
	v_cvt_pk_fp8_f32 v37, v38, v39 op_sel:[0,0,1]
	v_lshl_add_u64 v[26:27], s[10:11], 0, v[34:35]
	v_cvt_pk_fp8_f32 v28, v24, v25 op_sel:[0,0,1]
	v_cvt_pk_fp8_f32 v29, v32, v33 op_sel:[0,0,1]
	global_store_dwordx2 v[26:27], v[36:37], off
	v_cvt_pk_bf16_f32 v18, v22, v23
	v_cvt_pk_bf16_f32 v19, v24, v25
	v_cvt_pk_bf16_f32 v20, v20, v21
	v_cvt_pk_bf16_f32 v21, v32, v33
	global_store_dwordx4 v[30:31], v[18:21], off offset:256
	global_store_dwordx2 v[26:27], v[28:29], off offset:128
	v_lshlrev_b32_e32 v22, 16, v237
	v_lshlrev_b32_e32 v20, 16, v236
	v_and_b32_e32 v21, 0xffff0000, v236
	v_and_b32_e32 v23, 0xffff0000, v237
	v_pk_add_f32 v[16:17], v[16:17], v[22:23]
	v_pk_add_f32 v[14:15], v[14:15], v[20:21]
	v_lshlrev_b32_e32 v20, 16, v238
	v_and_b32_e32 v21, 0xffff0000, v238
	v_lshlrev_b32_e32 v22, 16, v239
	v_and_b32_e32 v23, 0xffff0000, v239
	v_pk_add_f32 v[22:23], v[12:13], v[22:23]
	v_pk_add_f32 v[12:13], v[10:11], v[20:21]
	v_mov_b32_e32 v20, v139
	v_cvt_pk_fp8_f32 v20, v14, v15
	v_lshlrev_b64 v[18:19], 11, v[82:83]
	v_lshl_add_u64 v[18:19], v[18:19], 0, v[140:141]
	v_mov_b32_e32 v21, v139
	v_cvt_pk_bf16_f32 v10, v14, v15
	v_cvt_pk_bf16_f32 v11, v16, v17
	v_cvt_pk_fp8_f32 v21, v12, v13
	v_cvt_pk_bf16_f32 v12, v12, v13
	v_cvt_pk_bf16_f32 v13, v22, v23
	v_lshl_add_u64 v[14:15], v[18:19], 1, s[8:9]
	v_cvt_pk_fp8_f32 v20, v16, v17 op_sel:[0,0,1]
	global_store_dwordx4 v[14:15], v[10:13], off
	v_lshlrev_b32_e32 v16, 16, v241
	v_and_b32_e32 v17, 0xffff0000, v241
	v_lshlrev_b32_e32 v12, 16, v240
	v_and_b32_e32 v13, 0xffff0000, v240
	v_pk_add_f32 v[8:9], v[8:9], v[16:17]
	v_pk_add_f32 v[6:7], v[6:7], v[12:13]
	v_lshlrev_b32_e32 v12, 16, v242
	v_and_b32_e32 v13, 0xffff0000, v242
	v_lshlrev_b32_e32 v16, 16, v243
	v_and_b32_e32 v17, 0xffff0000, v243
	v_pk_add_f32 v[16:17], v[4:5], v[16:17]
	v_pk_add_f32 v[4:5], v[2:3], v[12:13]
	v_mov_b32_e32 v12, v139
	v_mov_b32_e32 v13, v139
	v_cvt_pk_fp8_f32 v12, v6, v7
	v_cvt_pk_fp8_f32 v13, v4, v5
	v_cvt_pk_fp8_f32 v21, v22, v23 op_sel:[0,0,1]
	v_lshl_add_u64 v[10:11], s[10:11], 0, v[18:19]
	v_cvt_pk_fp8_f32 v12, v8, v9 op_sel:[0,0,1]
	v_cvt_pk_fp8_f32 v13, v16, v17 op_sel:[0,0,1]
	global_store_dwordx2 v[10:11], v[20:21], off
	v_cvt_pk_bf16_f32 v2, v6, v7
	v_cvt_pk_bf16_f32 v3, v8, v9
	v_cvt_pk_bf16_f32 v4, v4, v5
	v_cvt_pk_bf16_f32 v5, v16, v17
	global_store_dwordx4 v[14:15], v[2:5], off offset:256
	global_store_dwordx2 v[10:11], v[12:13], off offset:128
	s_cbranch_vccnz .LBB5_1397
	s_andn2_b64 vcc, exec, s[4:5]
	s_cbranch_vccnz .LBB5_1396
	s_barrier
	s_branch .LBB5_1396
